# plus: static s_setprio 1 for waves 4-7 during the GQA attention phase
# speedup vs baseline: 1.0111x; 1.0016x over previous
.LBB0_871:
	v_writelane_b32 v252, s96, 34
	s_mov_b64 s[90:91], s[92:93]
	s_andn2_b64 vcc, exec, s[86:87]
	v_writelane_b32 v252, s97, 35
	s_nop 0
	v_readlane_b32 s29, v252, 17
	s_cbranch_vccnz .LBB0_889
	v_readlane_b32 s2, v251, 4
	s_nop 3
	s_cmp_lt_u32 s2, 4
	s_cbranch_scc1 .Lgqa_prio_skip
	s_setprio 1
.Lgqa_prio_skip:
	v_cvt_f32_ubyte0_e32 v0, s89
	v_rcp_iflag_f32_e32 v0, v0
	s_and_b64 s[2:3], s[0:1], exec
	s_cselect_b32 s2, 0x200, 0
	s_add_u32 s58, s82, s2
	s_mul_i32 s72, s62, s29
	v_mul_f32_e32 v0, 0x4f7ffffe, v0
	s_addc_u32 s59, s83, 0
	s_lshl_b64 s[92:93], s[72:73], 1
	v_cvt_u32_f32_e32 v0, v0
	s_add_u32 s21, s66, s92
	s_addc_u32 s22, s67, s93
	s_add_u32 s23, s85, s92
	s_addc_u32 s24, s81, s93
	s_sub_i32 s2, 0, s89
	v_readfirstlane_b32 s3, v0
	s_mul_i32 s2, s2, s3
	s_mov_b32 s63, s73
	s_mul_hi_u32 s2, s3, s2
	s_lshl_b64 s[96:97], s[62:63], 7
	s_add_i32 s25, s3, s2
	s_lshl_b32 s38, s62, 5
	s_mul_i32 s3, s62, 0x180
	s_mul_hi_u32 s2, s62, 0x180
	s_add_u32 s6, s10, s3
	s_addc_u32 s7, s11, s2
	s_add_u32 s64, s64, s6
	s_addc_u32 s65, s65, s7
	s_lshl_b64 s[6:7], s[62:63], 8
	s_add_u32 s66, s66, s3
	s_mov_b32 s20, 0
	s_addc_u32 s67, s67, s2
	s_mov_b32 s3, s94
	s_branch .LBB0_874

.LBB0_889:
	s_setprio 0
	v_readlane_b32 s38, v255, 42
	v_readlane_b32 s28, v255, 44
	s_mov_b64 s[92:93], s[90:91]
	v_readlane_b32 s90, v255, 34
	v_readlane_b32 s96, v252, 34
	v_readlane_b32 s39, v255, 43
	v_readlane_b32 s29, v255, 45
	v_readlane_b32 s91, v255, 35
	v_readlane_b32 s97, v252, 35
	s_waitcnt vmcnt(0)
	s_barrier
